# adds the peeled first K-iteration (SrcC=0, no accumulator zeroing) to the RWKV LoRA-2 GEMM loop as well
# speedup vs baseline: 1.0224x; 1.0034x over previous
.LBB0_572:
	s_mov_b64 s[52:53], 0
	s_mov_b64 s[48:49], -1
	s_mov_b64 s[50:51], 0
.Lpeelg2a_hdr:
	s_add_u32 s58, s46, s52
	s_addc_u32 s59, s47, s53
	s_add_u32 s54, s58, 0x100
	s_addc_u32 s55, s59, 0
	s_and_b64 s[0:1], s[50:51], exec
	s_cselect_b32 s54, s40, s54
	s_cselect_b32 s55, s41, s55
	s_add_u32 s0, s44, s52
	s_addc_u32 s1, s45, s53
	s_add_u32 s52, s0, 0x100
	s_addc_u32 s53, s1, 0
	s_and_b64 s[0:1], s[50:51], exec
	s_cselect_b32 s57, s43, s53
	s_cselect_b32 s56, s42, s52
	s_add_i32 s51, 0, 0x10400
	s_add_i32 s84, s51, s60
	v_add_u32_e32 v146, s51, v172
	s_add_i32 m0, s61, 0xc400
	s_add_i32 s85, s61, 0xe400
	s_add_i32 s83, 0, 0x14400
	s_add_i32 s82, s84, 0x2000
	ds_read_b128 v[134:137], v146
	ds_read_b128 v[138:141], v146 offset:1024
	ds_read_b128 v[142:145], v146 offset:2048
	ds_read_b128 v[146:149], v146 offset:3072
	s_add_u32 s52, s56, 0x10000
	s_addc_u32 s53, s57, 0
	s_add_i32 s76, 0, 0x18400
	s_add_i32 s79, s83, s60
	s_add_i32 s75, s76, s60
	s_add_i32 s78, s79, 0x2000
	s_add_i32 s1, 0, 0x1c400
	s_add_i32 s0, s75, 0x2000
	s_add_u32 s50, s56, 0x10080
	s_addc_u32 s51, s57, 0
	s_add_i32 s81, s1, s60
	s_add_i32 s80, s81, 0x2000
	v_lshl_add_u64 v[180:181], s[58:59], 0, v[152:153]
	v_lshl_add_u64 v[180:181], v[180:181], 0, s[22:23]
	ds_read_b128 v[156:159], v174 offset:1024
	ds_read_b128 v[160:163], v174 offset:2048
	ds_read_b128 v[164:167], v174 offset:3072
	ds_read_b128 v[168:171], v174 offset:4096
	ds_read_b128 v[176:179], v174 offset:5120
	ds_read_b128 v[184:187], v174 offset:6144
	ds_read_b128 v[188:191], v174 offset:7168
	ds_read_b128 v[192:195], v174 offset:8192
	global_load_lds_dwordx4 v[180:181], off
	v_lshl_add_u64 v[180:181], s[58:59], 0, v[154:155]
	v_lshl_add_u64 v[180:181], v[180:181], 0, s[22:23]
	s_mov_b32 m0, s85
	s_nop 0
	global_load_lds_dwordx4 v[180:181], off
	s_waitcnt lgkmcnt(8)
	s_barrier
	s_waitcnt lgkmcnt(0)
	s_setprio 1
	s_waitcnt lgkmcnt(0)
	v_mfma_f32_16x16x32_bf16 v[130:133], v[134:137], v[156:159], 0
	v_mfma_f32_16x16x32_bf16 v[100:103], v[142:145], v[156:159], 0
	v_mfma_f32_16x16x32_bf16 v[126:129], v[134:137], v[164:167], 0
	v_mfma_f32_16x16x32_bf16 v[92:95], v[142:145], v[164:167], 0
	v_mfma_f32_16x16x32_bf16 v[122:125], v[134:137], v[176:179], 0
	v_mfma_f32_16x16x32_bf16 v[88:91], v[142:145], v[176:179], 0
	v_mfma_f32_16x16x32_bf16 v[118:121], v[134:137], v[188:191], 0
	v_mfma_f32_16x16x32_bf16 v[84:87], v[142:145], v[188:191], 0
	v_mfma_f32_16x16x32_bf16 v[130:133], v[138:141], v[160:163], v[130:133]
	v_mfma_f32_16x16x32_bf16 v[100:103], v[146:149], v[160:163], v[100:103]
	v_mfma_f32_16x16x32_bf16 v[126:129], v[138:141], v[168:171], v[126:129]
	v_mfma_f32_16x16x32_bf16 v[92:95], v[146:149], v[168:171], v[92:95]
	v_mfma_f32_16x16x32_bf16 v[122:125], v[138:141], v[184:187], v[122:125]
	v_mfma_f32_16x16x32_bf16 v[88:91], v[146:149], v[184:187], v[88:91]
	v_mfma_f32_16x16x32_bf16 v[118:121], v[138:141], v[192:195], v[118:121]
	v_mfma_f32_16x16x32_bf16 v[84:87], v[146:149], v[192:195], v[84:87]
	s_setprio 0
	s_barrier
	s_mov_b32 m0, s84
	v_add_u32_e32 v175, s83, v172
	v_lshl_add_u64 v[180:181], s[56:57], 0, v[2:3]
	ds_read_b128 v[196:199], v175
	ds_read_b128 v[200:203], v175 offset:1024
	ds_read_b128 v[204:207], v175 offset:2048
	ds_read_b128 v[208:211], v175 offset:3072
	global_load_lds_dwordx4 v[180:181], off
	v_lshl_add_u64 v[182:183], s[56:57], 0, v[150:151]
	s_mov_b32 m0, s82
	s_nop 0
	global_load_lds_dwordx4 v[182:183], off
	s_barrier
	s_waitcnt lgkmcnt(0)
	s_setprio 1
	s_waitcnt lgkmcnt(0)
	v_mfma_f32_16x16x32_bf16 v[68:71], v[196:199], v[156:159], 0
	v_mfma_f32_16x16x32_bf16 v[32:35], v[204:207], v[156:159], 0
	v_mfma_f32_16x16x32_bf16 v[60:63], v[196:199], v[164:167], 0
	v_mfma_f32_16x16x32_bf16 v[28:31], v[204:207], v[164:167], 0
	v_mfma_f32_16x16x32_bf16 v[56:59], v[196:199], v[176:179], 0
	v_mfma_f32_16x16x32_bf16 v[24:27], v[204:207], v[176:179], 0
	v_mfma_f32_16x16x32_bf16 v[52:55], v[196:199], v[188:191], 0
	v_mfma_f32_16x16x32_bf16 v[20:23], v[204:207], v[188:191], 0
	v_mfma_f32_16x16x32_bf16 v[68:71], v[200:203], v[160:163], v[68:71]
	v_mfma_f32_16x16x32_bf16 v[32:35], v[208:211], v[160:163], v[32:35]
	v_mfma_f32_16x16x32_bf16 v[60:63], v[200:203], v[168:171], v[60:63]
	v_mfma_f32_16x16x32_bf16 v[28:31], v[208:211], v[168:171], v[28:31]
	v_mfma_f32_16x16x32_bf16 v[56:59], v[200:203], v[184:187], v[56:59]
	v_mfma_f32_16x16x32_bf16 v[24:27], v[208:211], v[184:187], v[24:27]
	v_mfma_f32_16x16x32_bf16 v[52:55], v[200:203], v[192:195], v[52:55]
	v_mfma_f32_16x16x32_bf16 v[20:23], v[208:211], v[192:195], v[20:23]
	s_setprio 0
	s_mov_b32 m0, s62
	v_lshl_add_u64 v[212:213], s[54:55], 0, v[2:3]
	s_barrier
	ds_read_b128 v[156:159], v174 offset:17408
	ds_read_b128 v[160:163], v174 offset:18432
	ds_read_b128 v[164:167], v174 offset:19456
	ds_read_b128 v[168:171], v174 offset:20480
	ds_read_b128 v[176:179], v174 offset:21504
	ds_read_b128 v[184:187], v174 offset:22528
	ds_read_b128 v[188:191], v174 offset:23552
	ds_read_b128 v[192:195], v174 offset:24576
	global_load_lds_dwordx4 v[212:213], off
	v_lshl_add_u64 v[214:215], s[54:55], 0, v[150:151]
	s_mov_b32 m0, s63
	s_nop 0
	global_load_lds_dwordx4 v[214:215], off
	s_barrier
	s_waitcnt lgkmcnt(0)
	s_setprio 1
	s_waitcnt lgkmcnt(0)
	v_mfma_f32_16x16x32_bf16 v[112:115], v[134:137], v[156:159], 0
	v_mfma_f32_16x16x32_bf16 v[80:83], v[142:145], v[156:159], 0
	v_mfma_f32_16x16x32_bf16 v[108:111], v[134:137], v[164:167], 0
	v_mfma_f32_16x16x32_bf16 v[76:79], v[142:145], v[164:167], 0
	v_mfma_f32_16x16x32_bf16 v[104:107], v[134:137], v[176:179], 0
	v_mfma_f32_16x16x32_bf16 v[72:75], v[142:145], v[176:179], 0
	v_mfma_f32_16x16x32_bf16 v[96:99], v[134:137], v[188:191], 0
	v_mfma_f32_16x16x32_bf16 v[64:67], v[142:145], v[188:191], 0
	v_mfma_f32_16x16x32_bf16 v[112:115], v[138:141], v[160:163], v[112:115]
	v_mfma_f32_16x16x32_bf16 v[80:83], v[146:149], v[160:163], v[80:83]
	v_mfma_f32_16x16x32_bf16 v[108:111], v[138:141], v[168:171], v[108:111]
	v_mfma_f32_16x16x32_bf16 v[76:79], v[146:149], v[168:171], v[76:79]
	v_mfma_f32_16x16x32_bf16 v[104:107], v[138:141], v[184:187], v[104:107]
	v_mfma_f32_16x16x32_bf16 v[72:75], v[146:149], v[184:187], v[72:75]
	v_mfma_f32_16x16x32_bf16 v[96:99], v[138:141], v[192:195], v[96:99]
	v_mfma_f32_16x16x32_bf16 v[64:67], v[146:149], v[192:195], v[64:67]
	s_setprio 0
	s_barrier
	s_mov_b32 m0, s79
	v_lshl_add_u64 v[134:135], s[52:53], 0, v[2:3]
	global_load_lds_dwordx4 v[134:135], off
	v_lshl_add_u64 v[134:135], s[52:53], 0, v[150:151]
	s_mov_b32 m0, s78
	s_nop 0
	global_load_lds_dwordx4 v[134:135], off
	s_waitcnt vmcnt(6)
	s_barrier
	s_setprio 1
	v_mfma_f32_16x16x32_bf16 v[44:47], v[196:199], v[156:159], 0
	v_mfma_f32_16x16x32_bf16 v[12:15], v[204:207], v[156:159], 0
	v_mfma_f32_16x16x32_bf16 v[36:39], v[196:199], v[164:167], 0
	v_mfma_f32_16x16x32_bf16 v[4:7], v[204:207], v[164:167], 0
	v_mfma_f32_16x16x32_bf16 v[48:51], v[196:199], v[176:179], 0
	v_mfma_f32_16x16x32_bf16 v[16:19], v[204:207], v[176:179], 0
	v_mfma_f32_16x16x32_bf16 v[40:43], v[196:199], v[188:191], 0
	v_mfma_f32_16x16x32_bf16 v[8:11], v[204:207], v[188:191], 0
	v_mfma_f32_16x16x32_bf16 v[44:47], v[200:203], v[160:163], v[44:47]
	v_mfma_f32_16x16x32_bf16 v[12:15], v[208:211], v[160:163], v[12:15]
	v_mfma_f32_16x16x32_bf16 v[36:39], v[200:203], v[168:171], v[36:39]
	v_mfma_f32_16x16x32_bf16 v[4:7], v[208:211], v[168:171], v[4:7]
	v_mfma_f32_16x16x32_bf16 v[48:51], v[200:203], v[184:187], v[48:51]
	v_mfma_f32_16x16x32_bf16 v[16:19], v[208:211], v[184:187], v[16:19]
	v_mfma_f32_16x16x32_bf16 v[40:43], v[200:203], v[192:195], v[40:43]
	v_mfma_f32_16x16x32_bf16 v[8:11], v[208:211], v[192:195], v[8:11]
	s_setprio 0
	v_add_u32_e32 v146, s76, v172
	s_barrier
	ds_read_b128 v[134:137], v146
	ds_read_b128 v[138:141], v146 offset:1024
	ds_read_b128 v[142:145], v146 offset:2048
	ds_read_b128 v[146:149], v146 offset:3072
	s_mov_b32 m0, s64
	v_lshl_add_u64 v[196:197], s[54:55], 0, v[152:153]
	ds_read_b128 v[156:159], v174 offset:33792
	ds_read_b128 v[160:163], v174 offset:34816
	ds_read_b128 v[164:167], v174 offset:35840
	ds_read_b128 v[168:171], v174 offset:36864
	ds_read_b128 v[176:179], v174 offset:37888
	ds_read_b128 v[184:187], v174 offset:38912
	ds_read_b128 v[188:191], v174 offset:39936
	ds_read_b128 v[192:195], v174 offset:40960
	global_load_lds_dwordx4 v[196:197], off
	v_lshl_add_u64 v[196:197], s[54:55], 0, v[154:155]
	s_mov_b32 m0, s65
	s_nop 0
	global_load_lds_dwordx4 v[196:197], off
	s_waitcnt lgkmcnt(8)
	s_barrier
	s_waitcnt lgkmcnt(0)
	s_setprio 1
	s_waitcnt lgkmcnt(0)
	v_mfma_f32_16x16x32_bf16 v[130:133], v[134:137], v[156:159], v[130:133]
	v_mfma_f32_16x16x32_bf16 v[100:103], v[142:145], v[156:159], v[100:103]
	v_mfma_f32_16x16x32_bf16 v[126:129], v[134:137], v[164:167], v[126:129]
	v_mfma_f32_16x16x32_bf16 v[92:95], v[142:145], v[164:167], v[92:95]
	v_mfma_f32_16x16x32_bf16 v[122:125], v[134:137], v[176:179], v[122:125]
	v_mfma_f32_16x16x32_bf16 v[88:91], v[142:145], v[176:179], v[88:91]
	v_mfma_f32_16x16x32_bf16 v[118:121], v[134:137], v[188:191], v[118:121]
	v_mfma_f32_16x16x32_bf16 v[84:87], v[142:145], v[188:191], v[84:87]
	v_mfma_f32_16x16x32_bf16 v[130:133], v[138:141], v[160:163], v[130:133]
	v_mfma_f32_16x16x32_bf16 v[100:103], v[146:149], v[160:163], v[100:103]
	v_mfma_f32_16x16x32_bf16 v[126:129], v[138:141], v[168:171], v[126:129]
	v_mfma_f32_16x16x32_bf16 v[92:95], v[146:149], v[168:171], v[92:95]
	v_mfma_f32_16x16x32_bf16 v[122:125], v[138:141], v[184:187], v[122:125]
	v_mfma_f32_16x16x32_bf16 v[88:91], v[146:149], v[184:187], v[88:91]
	v_mfma_f32_16x16x32_bf16 v[118:121], v[138:141], v[192:195], v[118:121]
	v_mfma_f32_16x16x32_bf16 v[84:87], v[146:149], v[192:195], v[84:87]
	s_setprio 0
	s_barrier
	s_mov_b32 m0, s75
	v_add_u32_e32 v175, s1, v172
	v_lshl_add_u64 v[180:181], v[180:181], 0, s[22:23]
	ds_read_b128 v[196:199], v175
	ds_read_b128 v[200:203], v175 offset:1024
	ds_read_b128 v[204:207], v175 offset:2048
	ds_read_b128 v[208:211], v175 offset:3072
	global_load_lds_dwordx4 v[180:181], off
	v_lshl_add_u64 v[180:181], v[182:183], 0, s[22:23]
	s_mov_b32 m0, s0
	s_nop 0
	global_load_lds_dwordx4 v[180:181], off
	s_barrier
	s_waitcnt lgkmcnt(0)
	s_setprio 1
	s_waitcnt lgkmcnt(0)
	v_mfma_f32_16x16x32_bf16 v[68:71], v[196:199], v[156:159], v[68:71]
	v_mfma_f32_16x16x32_bf16 v[32:35], v[204:207], v[156:159], v[32:35]
	v_mfma_f32_16x16x32_bf16 v[60:63], v[196:199], v[164:167], v[60:63]
	v_mfma_f32_16x16x32_bf16 v[28:31], v[204:207], v[164:167], v[28:31]
	v_mfma_f32_16x16x32_bf16 v[56:59], v[196:199], v[176:179], v[56:59]
	v_mfma_f32_16x16x32_bf16 v[24:27], v[204:207], v[176:179], v[24:27]
	v_mfma_f32_16x16x32_bf16 v[52:55], v[196:199], v[188:191], v[52:55]
	v_mfma_f32_16x16x32_bf16 v[20:23], v[204:207], v[188:191], v[20:23]
	v_mfma_f32_16x16x32_bf16 v[68:71], v[200:203], v[160:163], v[68:71]
	v_mfma_f32_16x16x32_bf16 v[32:35], v[208:211], v[160:163], v[32:35]
	v_mfma_f32_16x16x32_bf16 v[60:63], v[200:203], v[168:171], v[60:63]
	v_mfma_f32_16x16x32_bf16 v[28:31], v[208:211], v[168:171], v[28:31]
	v_mfma_f32_16x16x32_bf16 v[56:59], v[200:203], v[184:187], v[56:59]
	v_mfma_f32_16x16x32_bf16 v[24:27], v[208:211], v[184:187], v[24:27]
	v_mfma_f32_16x16x32_bf16 v[52:55], v[200:203], v[192:195], v[52:55]
	v_mfma_f32_16x16x32_bf16 v[20:23], v[208:211], v[192:195], v[20:23]
	s_setprio 0
	s_mov_b32 m0, s70
	v_lshl_add_u64 v[180:181], v[212:213], 0, s[22:23]
	s_barrier
	ds_read_b128 v[156:159], v174 offset:50176
	ds_read_b128 v[160:163], v174 offset:51200
	ds_read_b128 v[164:167], v174 offset:52224
	ds_read_b128 v[168:171], v174 offset:53248
	ds_read_b128 v[176:179], v174 offset:54272
	ds_read_b128 v[184:187], v174 offset:55296
	ds_read_b128 v[188:191], v174 offset:56320
	ds_read_b128 v[192:195], v174 offset:57344
	global_load_lds_dwordx4 v[180:181], off
	v_lshl_add_u64 v[180:181], v[214:215], 0, s[22:23]
	s_mov_b32 m0, s71
	s_nop 0
	global_load_lds_dwordx4 v[180:181], off
	s_barrier
	s_waitcnt lgkmcnt(0)
	s_setprio 1
	s_waitcnt lgkmcnt(0)
	v_mfma_f32_16x16x32_bf16 v[112:115], v[134:137], v[156:159], v[112:115]
	v_mfma_f32_16x16x32_bf16 v[80:83], v[142:145], v[156:159], v[80:83]
	v_mfma_f32_16x16x32_bf16 v[108:111], v[134:137], v[164:167], v[108:111]
	v_mfma_f32_16x16x32_bf16 v[76:79], v[142:145], v[164:167], v[76:79]
	v_mfma_f32_16x16x32_bf16 v[104:107], v[134:137], v[176:179], v[104:107]
	v_mfma_f32_16x16x32_bf16 v[72:75], v[142:145], v[176:179], v[72:75]
	v_mfma_f32_16x16x32_bf16 v[96:99], v[134:137], v[188:191], v[96:99]
	v_mfma_f32_16x16x32_bf16 v[64:67], v[142:145], v[188:191], v[64:67]
	v_mfma_f32_16x16x32_bf16 v[112:115], v[138:141], v[160:163], v[112:115]
	v_mfma_f32_16x16x32_bf16 v[80:83], v[146:149], v[160:163], v[80:83]
	v_mfma_f32_16x16x32_bf16 v[108:111], v[138:141], v[168:171], v[108:111]
	v_mfma_f32_16x16x32_bf16 v[76:79], v[146:149], v[168:171], v[76:79]
	v_mfma_f32_16x16x32_bf16 v[104:107], v[138:141], v[184:187], v[104:107]
	v_mfma_f32_16x16x32_bf16 v[72:75], v[146:149], v[184:187], v[72:75]
	v_mfma_f32_16x16x32_bf16 v[96:99], v[138:141], v[192:195], v[96:99]
	v_mfma_f32_16x16x32_bf16 v[64:67], v[146:149], v[192:195], v[64:67]
	s_setprio 0
	s_barrier
	s_mov_b32 m0, s81
	v_lshl_add_u64 v[134:135], s[50:51], 0, v[2:3]
	global_load_lds_dwordx4 v[134:135], off
	v_lshl_add_u64 v[134:135], s[50:51], 0, v[150:151]
	s_mov_b32 m0, s80
	s_nop 0
	global_load_lds_dwordx4 v[134:135], off
	s_waitcnt vmcnt(6)
	s_barrier
	s_setprio 1
	v_mfma_f32_16x16x32_bf16 v[44:47], v[196:199], v[156:159], v[44:47]
	v_mfma_f32_16x16x32_bf16 v[12:15], v[204:207], v[156:159], v[12:15]
	v_mfma_f32_16x16x32_bf16 v[36:39], v[196:199], v[164:167], v[36:39]
	v_mfma_f32_16x16x32_bf16 v[4:7], v[204:207], v[164:167], v[4:7]
	v_mfma_f32_16x16x32_bf16 v[48:51], v[196:199], v[176:179], v[48:51]
	v_mfma_f32_16x16x32_bf16 v[16:19], v[204:207], v[176:179], v[16:19]
	v_mfma_f32_16x16x32_bf16 v[40:43], v[196:199], v[188:191], v[40:43]
	v_mfma_f32_16x16x32_bf16 v[8:11], v[204:207], v[188:191], v[8:11]
	v_mfma_f32_16x16x32_bf16 v[44:47], v[200:203], v[160:163], v[44:47]
	v_mfma_f32_16x16x32_bf16 v[12:15], v[208:211], v[160:163], v[12:15]
	v_mfma_f32_16x16x32_bf16 v[36:39], v[200:203], v[168:171], v[36:39]
	v_mfma_f32_16x16x32_bf16 v[4:7], v[208:211], v[168:171], v[4:7]
	v_mfma_f32_16x16x32_bf16 v[48:51], v[200:203], v[184:187], v[48:51]
	v_mfma_f32_16x16x32_bf16 v[16:19], v[208:211], v[184:187], v[16:19]
	v_mfma_f32_16x16x32_bf16 v[40:43], v[200:203], v[192:195], v[40:43]
	v_mfma_f32_16x16x32_bf16 v[8:11], v[208:211], v[192:195], v[8:11]
	s_setprio 0
	s_andn2_b64 vcc, exec, s[48:49]
	s_mov_b64 s[50:51], -1
	s_mov_b64 s[48:49], 0
	s_mov_b64 s[52:53], 0x100
	s_barrier
	s_cbranch_vccz .LBB0_573
	s_branch .Lpexit_g2a

.Lpexit_g2a:
	s_lshl_b32 s0, s3, 8
	v_lshl_add_u32 v134, s6, 8, v117
	s_and_b32 s0, s0, 0x300
	v_ashrrev_i32_e32 v135, 31, v134
	s_ashr_i32 s44, s3, 2
	v_or_b32_e32 v136, s0, v173
	v_lshlrev_b64 v[156:157], 10, v[134:135]
	v_or_b32_e32 v156, v156, v136
	s_mov_b64 s[0:1], -1
	s_cmp_gt_i32 s44, 1
	v_lshlrev_b32_e32 v175, 2, v136
	s_cbranch_scc0 .LBB0_576
	s_bfe_u32 s3, s3, 0x10002
	s_lshl_b32 s0, s3, 12
	s_add_u32 s0, s36, s0
	s_addc_u32 s1, s37, 0
	global_load_dwordx4 v[146:149], v175, s[0:1]
	global_load_dwordx4 v[142:145], v175, s[0:1] offset:64
	global_load_dwordx4 v[138:141], v175, s[0:1] offset:512
	global_load_dwordx4 v[134:137], v175, s[0:1] offset:576
	s_mul_i32 s3, s3, 0x4400000
	s_add_u32 s0, s68, s3
	s_addc_u32 s1, s69, 0
	s_waitcnt vmcnt(0)
	v_pk_add_f32 v[158:159], v[132:133], v[148:149]
	v_pk_add_f32 v[160:161], v[130:131], v[146:147]
	v_mul_f32_e32 v158, 0xbfb8aa3b, v158
	v_mul_f32_e32 v160, 0xbfb8aa3b, v160
	v_mul_f32_e32 v161, 0xbfb8aa3b, v161
	v_mul_f32_e32 v159, 0xbfb8aa3b, v159
	v_exp_f32_e32 v160, v160
	v_exp_f32_e32 v161, v161
	v_exp_f32_e32 v158, v158
	v_exp_f32_e32 v159, v159
	v_add_f32_e32 v160, 1.0, v160
	v_add_f32_e32 v161, 1.0, v161
	v_add_f32_e32 v158, 1.0, v158
	v_add_f32_e32 v159, 1.0, v159
	v_rcp_f32_e32 v160, v160
	v_rcp_f32_e32 v161, v161
	v_rcp_f32_e32 v162, v158
	v_rcp_f32_e32 v163, v159
	v_lshl_add_u64 v[158:159], v[156:157], 1, s[0:1]
	v_cvt_pk_bf16_f32 v160, v160, v161
	v_cvt_pk_bf16_f32 v161, v162, v163
	global_store_dwordx2 v[158:159], v[160:161], off
	v_pk_add_f32 v[160:161], v[126:127], v[146:147]
	s_nop 0
	v_mul_f32_e32 v160, 0xbfb8aa3b, v160
	v_exp_f32_e32 v162, v160
	v_mul_f32_e32 v160, 0xbfb8aa3b, v161
	v_exp_f32_e32 v163, v160
	v_pk_add_f32 v[160:161], v[128:129], v[148:149]
	v_add_f32_e32 v162, 1.0, v162
	v_mul_f32_e32 v160, 0xbfb8aa3b, v160
	v_mul_f32_e32 v161, 0xbfb8aa3b, v161
	v_exp_f32_e32 v160, v160
	v_exp_f32_e32 v161, v161
	v_add_f32_e32 v163, 1.0, v163
	v_rcp_f32_e32 v162, v162
	v_add_f32_e32 v160, 1.0, v160
	v_add_f32_e32 v161, 1.0, v161
	v_rcp_f32_e32 v163, v163
	v_rcp_f32_e32 v160, v160
	v_rcp_f32_e32 v161, v161
	v_cvt_pk_bf16_f32 v162, v162, v163
	v_cvt_pk_bf16_f32 v163, v160, v161
	v_add_co_u32_e32 v160, vcc, s31, v158
	s_nop 1
	v_addc_co_u32_e32 v161, vcc, 0, v159, vcc
	global_store_dwordx2 v[160:161], v[162:163], off
	v_pk_add_f32 v[162:163], v[122:123], v[146:147]
	s_mov_b32 s0, 0x10000
	v_mul_f32_e32 v162, 0xbfb8aa3b, v162
	v_exp_f32_e32 v164, v162
	v_mul_f32_e32 v162, 0xbfb8aa3b, v163
	v_exp_f32_e32 v165, v162
	v_pk_add_f32 v[162:163], v[124:125], v[148:149]
	v_add_f32_e32 v164, 1.0, v164
	v_mul_f32_e32 v162, 0xbfb8aa3b, v162
	v_mul_f32_e32 v163, 0xbfb8aa3b, v163
	v_exp_f32_e32 v162, v162
	v_exp_f32_e32 v163, v163
	v_add_f32_e32 v165, 1.0, v165
	v_rcp_f32_e32 v164, v164
	v_add_f32_e32 v162, 1.0, v162
	v_add_f32_e32 v163, 1.0, v163
	v_rcp_f32_e32 v165, v165
	v_rcp_f32_e32 v162, v162
	v_rcp_f32_e32 v163, v163
	v_cvt_pk_bf16_f32 v164, v164, v165
	v_cvt_pk_bf16_f32 v165, v162, v163
	v_add_co_u32_e32 v162, vcc, s0, v158
	s_nop 1
	v_addc_co_u32_e32 v163, vcc, 0, v159, vcc
	global_store_dwordx2 v[162:163], v[164:165], off
	v_pk_add_f32 v[164:165], v[118:119], v[146:147]
	s_mov_b32 s0, 0x18000
	v_mul_f32_e32 v164, 0xbfb8aa3b, v164
	v_exp_f32_e32 v166, v164
	v_mul_f32_e32 v164, 0xbfb8aa3b, v165
	v_exp_f32_e32 v167, v164
	v_pk_add_f32 v[164:165], v[120:121], v[148:149]
	v_add_f32_e32 v166, 1.0, v166
	v_mul_f32_e32 v164, 0xbfb8aa3b, v164
	v_mul_f32_e32 v165, 0xbfb8aa3b, v165
	v_exp_f32_e32 v164, v164
	v_exp_f32_e32 v165, v165
	v_add_f32_e32 v167, 1.0, v167
	v_rcp_f32_e32 v166, v166
	v_add_f32_e32 v164, 1.0, v164
	v_add_f32_e32 v165, 1.0, v165
	v_rcp_f32_e32 v167, v167
	v_rcp_f32_e32 v164, v164
	v_rcp_f32_e32 v165, v165
	v_cvt_pk_bf16_f32 v166, v166, v167
	v_cvt_pk_bf16_f32 v167, v164, v165
	v_add_co_u32_e32 v164, vcc, s0, v158
	s_nop 1
	v_addc_co_u32_e32 v165, vcc, 0, v159, vcc
	global_store_dwordx2 v[164:165], v[166:167], off
	v_pk_add_f32 v[166:167], v[112:113], v[146:147]
	s_nop 0
	v_mul_f32_e32 v166, 0xbfb8aa3b, v166
	v_exp_f32_e32 v168, v166
	v_mul_f32_e32 v166, 0xbfb8aa3b, v167
	v_exp_f32_e32 v169, v166
	v_pk_add_f32 v[166:167], v[114:115], v[148:149]
	v_add_f32_e32 v168, 1.0, v168
	v_mul_f32_e32 v166, 0xbfb8aa3b, v166
	v_mul_f32_e32 v167, 0xbfb8aa3b, v167
	v_exp_f32_e32 v166, v166
	v_exp_f32_e32 v167, v167
	v_add_f32_e32 v169, 1.0, v169
	v_rcp_f32_e32 v168, v168
	v_add_f32_e32 v166, 1.0, v166
	v_add_f32_e32 v167, 1.0, v167
	v_rcp_f32_e32 v169, v169
	v_rcp_f32_e32 v166, v166
	v_rcp_f32_e32 v167, v167
	v_cvt_pk_bf16_f32 v168, v168, v169
	v_cvt_pk_bf16_f32 v169, v166, v167
	v_add_co_u32_e32 v166, vcc, s16, v158
	s_nop 1
	v_addc_co_u32_e32 v167, vcc, 0, v159, vcc
	global_store_dwordx2 v[166:167], v[168:169], off
	v_pk_add_f32 v[168:169], v[108:109], v[146:147]
	s_mov_b32 s0, 0x48000
	v_mul_f32_e32 v168, 0xbfb8aa3b, v168
	v_exp_f32_e32 v170, v168
	v_mul_f32_e32 v168, 0xbfb8aa3b, v169
	v_exp_f32_e32 v171, v168
	v_pk_add_f32 v[168:169], v[110:111], v[148:149]
	v_add_f32_e32 v170, 1.0, v170
	v_mul_f32_e32 v168, 0xbfb8aa3b, v168
	v_mul_f32_e32 v169, 0xbfb8aa3b, v169
	v_exp_f32_e32 v168, v168
	v_exp_f32_e32 v169, v169
	v_add_f32_e32 v171, 1.0, v171
	v_rcp_f32_e32 v170, v170
	v_add_f32_e32 v168, 1.0, v168
	v_add_f32_e32 v169, 1.0, v169
	v_rcp_f32_e32 v171, v171
	v_rcp_f32_e32 v168, v168
	v_rcp_f32_e32 v169, v169
	v_cvt_pk_bf16_f32 v170, v170, v171
	v_cvt_pk_bf16_f32 v171, v168, v169
	v_add_co_u32_e32 v168, vcc, s0, v158
	s_nop 1
	v_addc_co_u32_e32 v169, vcc, 0, v159, vcc
	global_store_dwordx2 v[168:169], v[170:171], off
	v_pk_add_f32 v[170:171], v[104:105], v[146:147]
	s_mov_b32 s0, 0x50000
	v_mul_f32_e32 v170, 0xbfb8aa3b, v170
	v_exp_f32_e32 v176, v170
	v_mul_f32_e32 v170, 0xbfb8aa3b, v171
	v_exp_f32_e32 v177, v170
	v_pk_add_f32 v[170:171], v[106:107], v[148:149]
	v_add_f32_e32 v176, 1.0, v176
	v_mul_f32_e32 v170, 0xbfb8aa3b, v170
	v_mul_f32_e32 v171, 0xbfb8aa3b, v171
	v_exp_f32_e32 v170, v170
	v_exp_f32_e32 v171, v171
	v_add_f32_e32 v177, 1.0, v177
	v_rcp_f32_e32 v176, v176
	v_add_f32_e32 v170, 1.0, v170
	v_add_f32_e32 v171, 1.0, v171
	v_rcp_f32_e32 v177, v177
	v_rcp_f32_e32 v170, v170
	v_rcp_f32_e32 v171, v171
	v_cvt_pk_bf16_f32 v176, v176, v177
	v_cvt_pk_bf16_f32 v177, v170, v171
	v_add_co_u32_e32 v170, vcc, s0, v158
	s_nop 1
	v_addc_co_u32_e32 v171, vcc, 0, v159, vcc
	global_store_dwordx2 v[170:171], v[176:177], off
	v_pk_add_f32 v[146:147], v[96:97], v[146:147]
	s_mov_b32 s0, 0x58000
	v_mul_f32_e32 v146, 0xbfb8aa3b, v146
	v_exp_f32_e32 v176, v146
	v_mul_f32_e32 v146, 0xbfb8aa3b, v147
	v_exp_f32_e32 v177, v146
	v_pk_add_f32 v[146:147], v[98:99], v[148:149]
	v_add_f32_e32 v148, 1.0, v176
	v_mul_f32_e32 v146, 0xbfb8aa3b, v146
	v_mul_f32_e32 v147, 0xbfb8aa3b, v147
	v_exp_f32_e32 v146, v146
	v_exp_f32_e32 v147, v147
	v_add_f32_e32 v149, 1.0, v177
	v_rcp_f32_e32 v148, v148
	v_add_f32_e32 v146, 1.0, v146
	v_add_f32_e32 v147, 1.0, v147
	v_rcp_f32_e32 v149, v149
	v_rcp_f32_e32 v146, v146
	v_rcp_f32_e32 v147, v147
	v_cvt_pk_bf16_f32 v148, v148, v149
	v_cvt_pk_bf16_f32 v149, v146, v147
	v_add_co_u32_e32 v146, vcc, s0, v158
	s_nop 1
	v_addc_co_u32_e32 v147, vcc, 0, v159, vcc
	global_store_dwordx2 v[146:147], v[148:149], off
	v_pk_add_f32 v[148:149], v[100:101], v[142:143]
	s_nop 0
	v_mul_f32_e32 v148, 0xbfb8aa3b, v148
	v_exp_f32_e32 v176, v148
	v_mul_f32_e32 v148, 0xbfb8aa3b, v149
	v_exp_f32_e32 v177, v148
	v_pk_add_f32 v[148:149], v[102:103], v[144:145]
	v_add_f32_e32 v176, 1.0, v176
	v_mul_f32_e32 v148, 0xbfb8aa3b, v148
	v_exp_f32_e32 v148, v148
	v_mul_f32_e32 v149, 0xbfb8aa3b, v149
	v_exp_f32_e32 v149, v149
	v_add_f32_e32 v177, 1.0, v177
	v_add_f32_e32 v148, 1.0, v148
	v_rcp_f32_e32 v178, v148
	v_add_f32_e32 v148, 1.0, v149
	v_rcp_f32_e32 v176, v176
	v_rcp_f32_e32 v177, v177
	v_rcp_f32_e32 v149, v148
	v_cvt_pk_bf16_f32 v148, v176, v177
	v_cvt_pk_bf16_f32 v149, v178, v149
	global_store_dwordx2 v[158:159], v[148:149], off offset:32
	v_pk_add_f32 v[148:149], v[92:93], v[142:143]
	s_nop 0
	v_mul_f32_e32 v148, 0xbfb8aa3b, v148
	v_exp_f32_e32 v176, v148
	v_mul_f32_e32 v148, 0xbfb8aa3b, v149
	v_exp_f32_e32 v177, v148
	v_pk_add_f32 v[148:149], v[94:95], v[144:145]
	v_add_f32_e32 v176, 1.0, v176
	v_mul_f32_e32 v148, 0xbfb8aa3b, v148
	v_exp_f32_e32 v148, v148
	v_mul_f32_e32 v149, 0xbfb8aa3b, v149
	v_exp_f32_e32 v149, v149
	v_add_f32_e32 v177, 1.0, v177
	v_add_f32_e32 v148, 1.0, v148
	v_rcp_f32_e32 v178, v148
	v_add_f32_e32 v148, 1.0, v149
	v_rcp_f32_e32 v176, v176
	v_rcp_f32_e32 v177, v177
	v_rcp_f32_e32 v149, v148
	v_cvt_pk_bf16_f32 v148, v176, v177
	v_cvt_pk_bf16_f32 v149, v178, v149
	global_store_dwordx2 v[160:161], v[148:149], off offset:32
	v_pk_add_f32 v[148:149], v[88:89], v[142:143]
	s_nop 0
	v_mul_f32_e32 v148, 0xbfb8aa3b, v148
	v_exp_f32_e32 v176, v148
	v_mul_f32_e32 v148, 0xbfb8aa3b, v149
	v_exp_f32_e32 v177, v148
	v_pk_add_f32 v[148:149], v[90:91], v[144:145]
	v_add_f32_e32 v176, 1.0, v176
	v_mul_f32_e32 v148, 0xbfb8aa3b, v148
	v_exp_f32_e32 v148, v148
	v_mul_f32_e32 v149, 0xbfb8aa3b, v149
	v_exp_f32_e32 v149, v149
	v_add_f32_e32 v177, 1.0, v177
	v_add_f32_e32 v148, 1.0, v148
	v_rcp_f32_e32 v178, v148
	v_add_f32_e32 v148, 1.0, v149
	v_rcp_f32_e32 v176, v176
	v_rcp_f32_e32 v177, v177
	v_rcp_f32_e32 v149, v148
	v_cvt_pk_bf16_f32 v148, v176, v177
	v_cvt_pk_bf16_f32 v149, v178, v149
	global_store_dwordx2 v[162:163], v[148:149], off offset:32
	v_pk_add_f32 v[148:149], v[84:85], v[142:143]
	s_nop 0
	v_mul_f32_e32 v148, 0xbfb8aa3b, v148
	v_exp_f32_e32 v176, v148
	v_mul_f32_e32 v148, 0xbfb8aa3b, v149
	v_exp_f32_e32 v177, v148
	v_pk_add_f32 v[148:149], v[86:87], v[144:145]
	v_add_f32_e32 v176, 1.0, v176
	v_mul_f32_e32 v148, 0xbfb8aa3b, v148
	v_exp_f32_e32 v148, v148
	v_mul_f32_e32 v149, 0xbfb8aa3b, v149
	v_exp_f32_e32 v149, v149
	v_add_f32_e32 v177, 1.0, v177
	v_add_f32_e32 v148, 1.0, v148
	v_rcp_f32_e32 v178, v148
	v_add_f32_e32 v148, 1.0, v149
	v_rcp_f32_e32 v176, v176
	v_rcp_f32_e32 v177, v177
	v_rcp_f32_e32 v149, v148
	v_cvt_pk_bf16_f32 v148, v176, v177
	v_cvt_pk_bf16_f32 v149, v178, v149
	global_store_dwordx2 v[164:165], v[148:149], off offset:32
	v_pk_add_f32 v[148:149], v[80:81], v[142:143]
	s_nop 0
	v_mul_f32_e32 v148, 0xbfb8aa3b, v148
	v_exp_f32_e32 v176, v148
	v_mul_f32_e32 v148, 0xbfb8aa3b, v149
	v_exp_f32_e32 v177, v148
	v_pk_add_f32 v[148:149], v[82:83], v[144:145]
	v_add_f32_e32 v176, 1.0, v176
	v_mul_f32_e32 v148, 0xbfb8aa3b, v148
	v_exp_f32_e32 v148, v148
	v_mul_f32_e32 v149, 0xbfb8aa3b, v149
	v_exp_f32_e32 v149, v149
	v_add_f32_e32 v177, 1.0, v177
	v_add_f32_e32 v148, 1.0, v148
	v_rcp_f32_e32 v178, v148
	v_add_f32_e32 v148, 1.0, v149
	v_rcp_f32_e32 v176, v176
	v_rcp_f32_e32 v177, v177
	v_rcp_f32_e32 v149, v148
	v_cvt_pk_bf16_f32 v148, v176, v177
	v_cvt_pk_bf16_f32 v149, v178, v149
	global_store_dwordx2 v[166:167], v[148:149], off offset:32
	v_pk_add_f32 v[148:149], v[76:77], v[142:143]
	s_nop 0
	v_mul_f32_e32 v148, 0xbfb8aa3b, v148
	v_exp_f32_e32 v176, v148
	v_mul_f32_e32 v148, 0xbfb8aa3b, v149
	v_exp_f32_e32 v177, v148
	v_pk_add_f32 v[148:149], v[78:79], v[144:145]
	v_add_f32_e32 v176, 1.0, v176
	v_mul_f32_e32 v148, 0xbfb8aa3b, v148
	v_exp_f32_e32 v148, v148
	v_mul_f32_e32 v149, 0xbfb8aa3b, v149
	v_exp_f32_e32 v149, v149
	v_add_f32_e32 v177, 1.0, v177
	v_add_f32_e32 v148, 1.0, v148
	v_rcp_f32_e32 v178, v148
	v_add_f32_e32 v148, 1.0, v149
	v_rcp_f32_e32 v176, v176
	v_rcp_f32_e32 v177, v177
	v_rcp_f32_e32 v149, v148
	v_cvt_pk_bf16_f32 v148, v176, v177
	v_cvt_pk_bf16_f32 v149, v178, v149
	global_store_dwordx2 v[168:169], v[148:149], off offset:32
	v_pk_add_f32 v[148:149], v[72:73], v[142:143]
	s_nop 0
	v_mul_f32_e32 v148, 0xbfb8aa3b, v148
	v_exp_f32_e32 v176, v148
	v_mul_f32_e32 v148, 0xbfb8aa3b, v149
	v_exp_f32_e32 v177, v148
	v_pk_add_f32 v[148:149], v[74:75], v[144:145]
	v_add_f32_e32 v176, 1.0, v176
	v_mul_f32_e32 v148, 0xbfb8aa3b, v148
	v_exp_f32_e32 v148, v148
	v_mul_f32_e32 v149, 0xbfb8aa3b, v149
	v_exp_f32_e32 v149, v149
	v_add_f32_e32 v177, 1.0, v177
	v_add_f32_e32 v148, 1.0, v148
	v_rcp_f32_e32 v178, v148
	v_add_f32_e32 v148, 1.0, v149
	v_rcp_f32_e32 v176, v176
	v_rcp_f32_e32 v177, v177
	v_rcp_f32_e32 v149, v148
	v_cvt_pk_bf16_f32 v148, v176, v177
	v_cvt_pk_bf16_f32 v149, v178, v149
	global_store_dwordx2 v[170:171], v[148:149], off offset:32
	v_pk_add_f32 v[142:143], v[64:65], v[142:143]
	s_nop 0
	v_mul_f32_e32 v142, 0xbfb8aa3b, v142
	v_exp_f32_e32 v148, v142
	v_mul_f32_e32 v142, 0xbfb8aa3b, v143
	v_exp_f32_e32 v149, v142
	v_pk_add_f32 v[142:143], v[66:67], v[144:145]
	v_add_f32_e32 v144, 1.0, v148
	v_mul_f32_e32 v142, 0xbfb8aa3b, v142
	v_exp_f32_e32 v142, v142
	v_mul_f32_e32 v143, 0xbfb8aa3b, v143
	v_exp_f32_e32 v143, v143
	v_add_f32_e32 v145, 1.0, v149
	v_add_f32_e32 v142, 1.0, v142
	v_rcp_f32_e32 v148, v142
	v_add_f32_e32 v142, 1.0, v143
	v_rcp_f32_e32 v144, v144
	v_rcp_f32_e32 v145, v145
	v_rcp_f32_e32 v143, v142
	v_cvt_pk_bf16_f32 v142, v144, v145
	v_cvt_pk_bf16_f32 v143, v148, v143
	global_store_dwordx2 v[146:147], v[142:143], off offset:32
	v_pk_add_f32 v[142:143], v[68:69], v[138:139]
	s_nop 0
	v_mul_f32_e32 v142, 0xbfb8aa3b, v142
	v_exp_f32_e32 v144, v142
	v_mul_f32_e32 v142, 0xbfb8aa3b, v143
	v_exp_f32_e32 v145, v142
	v_pk_add_f32 v[142:143], v[70:71], v[140:141]
	v_add_f32_e32 v144, 1.0, v144
	v_mul_f32_e32 v142, 0xbfb8aa3b, v142
	v_exp_f32_e32 v142, v142
	v_mul_f32_e32 v143, 0xbfb8aa3b, v143
	v_exp_f32_e32 v143, v143
	v_add_f32_e32 v145, 1.0, v145
	v_add_f32_e32 v142, 1.0, v142
	v_rcp_f32_e32 v148, v142
	v_add_f32_e32 v142, 1.0, v143
	v_rcp_f32_e32 v144, v144
	v_rcp_f32_e32 v145, v145
	v_rcp_f32_e32 v143, v142
	v_cvt_pk_bf16_f32 v142, v144, v145
	v_cvt_pk_bf16_f32 v143, v148, v143
	global_store_dwordx2 v[158:159], v[142:143], off offset:256
	v_pk_add_f32 v[142:143], v[60:61], v[138:139]
	s_nop 0
	v_mul_f32_e32 v142, 0xbfb8aa3b, v142
	v_exp_f32_e32 v144, v142
	v_mul_f32_e32 v142, 0xbfb8aa3b, v143
	v_exp_f32_e32 v145, v142
	v_pk_add_f32 v[142:143], v[62:63], v[140:141]
	v_add_f32_e32 v144, 1.0, v144
	v_mul_f32_e32 v142, 0xbfb8aa3b, v142
	v_exp_f32_e32 v142, v142
	v_mul_f32_e32 v143, 0xbfb8aa3b, v143
	v_exp_f32_e32 v143, v143
	v_add_f32_e32 v145, 1.0, v145
	v_add_f32_e32 v142, 1.0, v142
	v_rcp_f32_e32 v148, v142
	v_add_f32_e32 v142, 1.0, v143
	v_rcp_f32_e32 v144, v144
	v_rcp_f32_e32 v145, v145
	v_rcp_f32_e32 v143, v142
	v_cvt_pk_bf16_f32 v142, v144, v145
	v_cvt_pk_bf16_f32 v143, v148, v143
	global_store_dwordx2 v[160:161], v[142:143], off offset:256
	v_pk_add_f32 v[142:143], v[56:57], v[138:139]
	s_nop 0
	v_mul_f32_e32 v142, 0xbfb8aa3b, v142
	v_exp_f32_e32 v144, v142
	v_mul_f32_e32 v142, 0xbfb8aa3b, v143
	v_exp_f32_e32 v145, v142
	v_pk_add_f32 v[142:143], v[58:59], v[140:141]
	v_add_f32_e32 v144, 1.0, v144
	v_mul_f32_e32 v142, 0xbfb8aa3b, v142
	v_exp_f32_e32 v142, v142
	v_mul_f32_e32 v143, 0xbfb8aa3b, v143
	v_exp_f32_e32 v143, v143
	v_add_f32_e32 v145, 1.0, v145
	v_add_f32_e32 v142, 1.0, v142
	v_rcp_f32_e32 v148, v142
	v_add_f32_e32 v142, 1.0, v143
	v_rcp_f32_e32 v144, v144
	v_rcp_f32_e32 v145, v145
	v_rcp_f32_e32 v143, v142
	v_cvt_pk_bf16_f32 v142, v144, v145
	v_cvt_pk_bf16_f32 v143, v148, v143
	global_store_dwordx2 v[162:163], v[142:143], off offset:256
	v_pk_add_f32 v[142:143], v[52:53], v[138:139]
	s_nop 0
	v_mul_f32_e32 v142, 0xbfb8aa3b, v142
	v_exp_f32_e32 v144, v142
	v_mul_f32_e32 v142, 0xbfb8aa3b, v143
	v_exp_f32_e32 v145, v142
	v_pk_add_f32 v[142:143], v[54:55], v[140:141]
	v_add_f32_e32 v144, 1.0, v144
	v_mul_f32_e32 v142, 0xbfb8aa3b, v142
	v_exp_f32_e32 v142, v142
	v_mul_f32_e32 v143, 0xbfb8aa3b, v143
	v_exp_f32_e32 v143, v143
	v_add_f32_e32 v145, 1.0, v145
	v_add_f32_e32 v142, 1.0, v142
	v_rcp_f32_e32 v148, v142
	v_add_f32_e32 v142, 1.0, v143
	v_rcp_f32_e32 v144, v144
	v_rcp_f32_e32 v145, v145
	v_rcp_f32_e32 v143, v142
	v_cvt_pk_bf16_f32 v142, v144, v145
	v_cvt_pk_bf16_f32 v143, v148, v143
	global_store_dwordx2 v[164:165], v[142:143], off offset:256
	v_pk_add_f32 v[142:143], v[44:45], v[138:139]
	s_nop 0
	v_mul_f32_e32 v142, 0xbfb8aa3b, v142
	v_exp_f32_e32 v144, v142
	v_mul_f32_e32 v142, 0xbfb8aa3b, v143
	v_exp_f32_e32 v145, v142
	v_pk_add_f32 v[142:143], v[46:47], v[140:141]
	v_add_f32_e32 v144, 1.0, v144
	v_mul_f32_e32 v142, 0xbfb8aa3b, v142
	v_exp_f32_e32 v142, v142
	v_mul_f32_e32 v143, 0xbfb8aa3b, v143
	v_exp_f32_e32 v143, v143
	v_add_f32_e32 v145, 1.0, v145
	v_add_f32_e32 v142, 1.0, v142
	v_rcp_f32_e32 v148, v142
	v_add_f32_e32 v142, 1.0, v143
	v_rcp_f32_e32 v144, v144
	v_rcp_f32_e32 v145, v145
	v_rcp_f32_e32 v143, v142
	v_cvt_pk_bf16_f32 v142, v144, v145
	v_cvt_pk_bf16_f32 v143, v148, v143
	global_store_dwordx2 v[166:167], v[142:143], off offset:256
	v_pk_add_f32 v[142:143], v[36:37], v[138:139]
	s_nop 0
	v_mul_f32_e32 v142, 0xbfb8aa3b, v142
	v_exp_f32_e32 v144, v142
	v_mul_f32_e32 v142, 0xbfb8aa3b, v143
	v_exp_f32_e32 v145, v142
	v_pk_add_f32 v[142:143], v[38:39], v[140:141]
	v_add_f32_e32 v144, 1.0, v144
	v_mul_f32_e32 v142, 0xbfb8aa3b, v142
	v_exp_f32_e32 v142, v142
	v_mul_f32_e32 v143, 0xbfb8aa3b, v143
	v_exp_f32_e32 v143, v143
	v_add_f32_e32 v145, 1.0, v145
	v_add_f32_e32 v142, 1.0, v142
	v_rcp_f32_e32 v148, v142
	v_add_f32_e32 v142, 1.0, v143
	v_rcp_f32_e32 v144, v144
	v_rcp_f32_e32 v145, v145
	v_rcp_f32_e32 v143, v142
	v_cvt_pk_bf16_f32 v142, v144, v145
	v_cvt_pk_bf16_f32 v143, v148, v143
	global_store_dwordx2 v[168:169], v[142:143], off offset:256
	v_pk_add_f32 v[142:143], v[48:49], v[138:139]
	s_nop 0
	v_mul_f32_e32 v142, 0xbfb8aa3b, v142
	v_exp_f32_e32 v144, v142
	v_mul_f32_e32 v142, 0xbfb8aa3b, v143
	v_exp_f32_e32 v145, v142
	v_pk_add_f32 v[142:143], v[50:51], v[140:141]
	v_add_f32_e32 v144, 1.0, v144
	v_mul_f32_e32 v142, 0xbfb8aa3b, v142
	v_exp_f32_e32 v142, v142
	v_mul_f32_e32 v143, 0xbfb8aa3b, v143
	v_exp_f32_e32 v143, v143
	v_add_f32_e32 v145, 1.0, v145
	v_add_f32_e32 v142, 1.0, v142
	v_rcp_f32_e32 v148, v142
	v_add_f32_e32 v142, 1.0, v143
	v_rcp_f32_e32 v144, v144
	v_rcp_f32_e32 v145, v145
	v_rcp_f32_e32 v143, v142
	v_cvt_pk_bf16_f32 v142, v144, v145
	v_cvt_pk_bf16_f32 v143, v148, v143
	global_store_dwordx2 v[170:171], v[142:143], off offset:256
	v_pk_add_f32 v[138:139], v[40:41], v[138:139]
	s_nop 0
	v_mul_f32_e32 v138, 0xbfb8aa3b, v138
	v_exp_f32_e32 v142, v138
	v_mul_f32_e32 v138, 0xbfb8aa3b, v139
	v_exp_f32_e32 v143, v138
	v_pk_add_f32 v[138:139], v[42:43], v[140:141]
	v_add_f32_e32 v140, 1.0, v142
	v_mul_f32_e32 v138, 0xbfb8aa3b, v138
	v_exp_f32_e32 v138, v138
	v_mul_f32_e32 v139, 0xbfb8aa3b, v139
	v_exp_f32_e32 v139, v139
	v_add_f32_e32 v141, 1.0, v143
	v_add_f32_e32 v138, 1.0, v138
	v_rcp_f32_e32 v142, v138
	v_add_f32_e32 v138, 1.0, v139
	v_rcp_f32_e32 v140, v140
	v_rcp_f32_e32 v141, v141
	v_rcp_f32_e32 v139, v138
	v_cvt_pk_bf16_f32 v138, v140, v141
	v_cvt_pk_bf16_f32 v139, v142, v139
	global_store_dwordx2 v[146:147], v[138:139], off offset:256
	v_pk_add_f32 v[138:139], v[32:33], v[134:135]
	s_nop 0
	v_mul_f32_e32 v138, 0xbfb8aa3b, v138
	v_exp_f32_e32 v140, v138
	v_mul_f32_e32 v138, 0xbfb8aa3b, v139
	v_exp_f32_e32 v141, v138
	v_pk_add_f32 v[138:139], v[34:35], v[136:137]
	v_add_f32_e32 v140, 1.0, v140
	v_mul_f32_e32 v138, 0xbfb8aa3b, v138
	v_exp_f32_e32 v138, v138
	v_mul_f32_e32 v139, 0xbfb8aa3b, v139
	v_exp_f32_e32 v139, v139
	v_add_f32_e32 v141, 1.0, v141
	v_add_f32_e32 v138, 1.0, v138
	v_rcp_f32_e32 v142, v138
	v_add_f32_e32 v138, 1.0, v139
	v_rcp_f32_e32 v140, v140
	v_rcp_f32_e32 v141, v141
	v_rcp_f32_e32 v139, v138
	v_cvt_pk_bf16_f32 v138, v140, v141
	v_cvt_pk_bf16_f32 v139, v142, v139
	global_store_dwordx2 v[158:159], v[138:139], off offset:288
	v_pk_add_f32 v[138:139], v[28:29], v[134:135]
	s_nop 0
	v_mul_f32_e32 v138, 0xbfb8aa3b, v138
	v_exp_f32_e32 v140, v138
	v_mul_f32_e32 v138, 0xbfb8aa3b, v139
	v_exp_f32_e32 v141, v138
	v_pk_add_f32 v[138:139], v[30:31], v[136:137]
	v_add_f32_e32 v140, 1.0, v140
	v_mul_f32_e32 v138, 0xbfb8aa3b, v138
	v_exp_f32_e32 v138, v138
	v_mul_f32_e32 v139, 0xbfb8aa3b, v139
	v_exp_f32_e32 v139, v139
	v_add_f32_e32 v141, 1.0, v141
	v_add_f32_e32 v138, 1.0, v138
	v_rcp_f32_e32 v142, v138
	v_add_f32_e32 v138, 1.0, v139
	v_rcp_f32_e32 v140, v140
	v_rcp_f32_e32 v141, v141
	v_rcp_f32_e32 v139, v138
	v_cvt_pk_bf16_f32 v138, v140, v141
	v_cvt_pk_bf16_f32 v139, v142, v139
	global_store_dwordx2 v[160:161], v[138:139], off offset:288
	v_pk_add_f32 v[138:139], v[24:25], v[134:135]
	s_nop 0
	v_mul_f32_e32 v138, 0xbfb8aa3b, v138
	v_exp_f32_e32 v140, v138
	v_mul_f32_e32 v138, 0xbfb8aa3b, v139
	v_exp_f32_e32 v141, v138
	v_pk_add_f32 v[138:139], v[26:27], v[136:137]
	v_add_f32_e32 v140, 1.0, v140
	v_mul_f32_e32 v138, 0xbfb8aa3b, v138
	v_exp_f32_e32 v138, v138
	v_mul_f32_e32 v139, 0xbfb8aa3b, v139
	v_exp_f32_e32 v139, v139
	v_add_f32_e32 v141, 1.0, v141
	v_add_f32_e32 v138, 1.0, v138
	v_rcp_f32_e32 v142, v138
	v_add_f32_e32 v138, 1.0, v139
	v_rcp_f32_e32 v140, v140
	v_rcp_f32_e32 v141, v141
	v_rcp_f32_e32 v139, v138
	v_cvt_pk_bf16_f32 v138, v140, v141
	v_cvt_pk_bf16_f32 v139, v142, v139
	global_store_dwordx2 v[162:163], v[138:139], off offset:288
	v_pk_add_f32 v[138:139], v[20:21], v[134:135]
	s_nop 0
	v_mul_f32_e32 v138, 0xbfb8aa3b, v138
	v_exp_f32_e32 v140, v138
	v_mul_f32_e32 v138, 0xbfb8aa3b, v139
	v_exp_f32_e32 v141, v138
	v_pk_add_f32 v[138:139], v[22:23], v[136:137]
	v_add_f32_e32 v140, 1.0, v140
	v_mul_f32_e32 v138, 0xbfb8aa3b, v138
	v_exp_f32_e32 v138, v138
	v_mul_f32_e32 v139, 0xbfb8aa3b, v139
	v_exp_f32_e32 v139, v139
	v_add_f32_e32 v141, 1.0, v141
	v_add_f32_e32 v138, 1.0, v138
	v_rcp_f32_e32 v142, v138
	v_add_f32_e32 v138, 1.0, v139
	v_rcp_f32_e32 v140, v140
	v_rcp_f32_e32 v141, v141
	v_rcp_f32_e32 v139, v138
	v_cvt_pk_bf16_f32 v138, v140, v141
	v_cvt_pk_bf16_f32 v139, v142, v139
	global_store_dwordx2 v[164:165], v[138:139], off offset:288
	v_pk_add_f32 v[138:139], v[12:13], v[134:135]
	s_nop 0
	v_mul_f32_e32 v138, 0xbfb8aa3b, v138
	v_exp_f32_e32 v140, v138
	v_mul_f32_e32 v138, 0xbfb8aa3b, v139
	v_exp_f32_e32 v141, v138
	v_pk_add_f32 v[138:139], v[14:15], v[136:137]
	v_add_f32_e32 v140, 1.0, v140
	v_mul_f32_e32 v138, 0xbfb8aa3b, v138
	v_exp_f32_e32 v138, v138
	v_mul_f32_e32 v139, 0xbfb8aa3b, v139
	v_exp_f32_e32 v139, v139
	v_add_f32_e32 v141, 1.0, v141
	v_add_f32_e32 v138, 1.0, v138
	v_rcp_f32_e32 v142, v138
	v_add_f32_e32 v138, 1.0, v139
	v_rcp_f32_e32 v140, v140
	v_rcp_f32_e32 v141, v141
	v_rcp_f32_e32 v139, v138
	v_cvt_pk_bf16_f32 v138, v140, v141
	v_cvt_pk_bf16_f32 v139, v142, v139
	global_store_dwordx2 v[166:167], v[138:139], off offset:288
	v_pk_add_f32 v[138:139], v[4:5], v[134:135]
	s_nop 0
	v_mul_f32_e32 v138, 0xbfb8aa3b, v138
	v_exp_f32_e32 v140, v138
	v_mul_f32_e32 v138, 0xbfb8aa3b, v139
	v_exp_f32_e32 v141, v138
	v_pk_add_f32 v[138:139], v[6:7], v[136:137]
	v_add_f32_e32 v140, 1.0, v140
	v_mul_f32_e32 v138, 0xbfb8aa3b, v138
	v_exp_f32_e32 v138, v138
	v_mul_f32_e32 v139, 0xbfb8aa3b, v139
	v_exp_f32_e32 v139, v139
	v_add_f32_e32 v141, 1.0, v141
	v_add_f32_e32 v138, 1.0, v138
	v_rcp_f32_e32 v142, v138
	v_add_f32_e32 v138, 1.0, v139
	v_rcp_f32_e32 v140, v140
	v_rcp_f32_e32 v141, v141
	v_rcp_f32_e32 v139, v138
	v_cvt_pk_bf16_f32 v138, v140, v141
	v_cvt_pk_bf16_f32 v139, v142, v139
	global_store_dwordx2 v[168:169], v[138:139], off offset:288
	v_pk_add_f32 v[138:139], v[16:17], v[134:135]
	s_nop 0
	v_mul_f32_e32 v138, 0xbfb8aa3b, v138
	v_exp_f32_e32 v140, v138
	v_mul_f32_e32 v138, 0xbfb8aa3b, v139
	v_exp_f32_e32 v141, v138
	v_pk_add_f32 v[138:139], v[18:19], v[136:137]
	v_add_f32_e32 v140, 1.0, v140
	v_mul_f32_e32 v138, 0xbfb8aa3b, v138
	v_exp_f32_e32 v138, v138
	v_mul_f32_e32 v139, 0xbfb8aa3b, v139
	v_exp_f32_e32 v139, v139
	v_add_f32_e32 v141, 1.0, v141
	v_add_f32_e32 v138, 1.0, v138
	v_rcp_f32_e32 v142, v138
	v_add_f32_e32 v138, 1.0, v139
	v_rcp_f32_e32 v140, v140
	v_rcp_f32_e32 v141, v141
	v_rcp_f32_e32 v139, v138
	v_cvt_pk_bf16_f32 v138, v140, v141
	v_cvt_pk_bf16_f32 v139, v142, v139
	global_store_dwordx2 v[170:171], v[138:139], off offset:288
	v_pk_add_f32 v[134:135], v[8:9], v[134:135]
	s_nop 0
	v_mul_f32_e32 v134, 0xbfb8aa3b, v134
	v_exp_f32_e32 v138, v134
	v_mul_f32_e32 v134, 0xbfb8aa3b, v135
	v_exp_f32_e32 v139, v134
	v_pk_add_f32 v[134:135], v[10:11], v[136:137]
	v_add_f32_e32 v136, 1.0, v138
	v_mul_f32_e32 v134, 0xbfb8aa3b, v134
	v_exp_f32_e32 v134, v134
	v_mul_f32_e32 v135, 0xbfb8aa3b, v135
	v_exp_f32_e32 v135, v135
	v_add_f32_e32 v137, 1.0, v139
	v_add_f32_e32 v134, 1.0, v134
	v_rcp_f32_e32 v138, v134
	v_add_f32_e32 v134, 1.0, v135
	v_rcp_f32_e32 v136, v136
	v_rcp_f32_e32 v137, v137
	v_rcp_f32_e32 v135, v134
	v_cvt_pk_bf16_f32 v134, v136, v137
	v_cvt_pk_bf16_f32 v135, v138, v135
	global_store_dwordx2 v[146:147], v[134:135], off offset:288
	s_mov_b64 s[0:1], 0
